# PRE fuse_ov: two 4-d groups per trip (38 loads in flight, 8 round trips per item)
# baseline (speedup 1.0000x reference)
.LBB0_49:
	s_add_u32 s82, s79, s4
	s_addc_u32 s83, s80, s5
	global_load_dwordx4 v[76:79], v[42:43], off offset:-268
	global_load_dwordx4 v[80:83], v[42:43], off offset:-12
	global_load_dwordx4 v[120:123], v3, s[82:83]
	global_load_dwordx4 v[116:119], v3, s[82:83] offset:16
	global_load_dwordx4 v[112:115], v3, s[82:83] offset:32
	global_load_dwordx4 v[108:111], v3, s[82:83] offset:48
	s_add_u32 s82, s44, s4
	s_addc_u32 s83, s45, s5
	global_load_dwordx4 v[130:133], v3, s[82:83]
	global_load_dwordx4 v[134:137], v3, s[82:83] offset:16
	global_load_dwordx4 v[138:141], v3, s[82:83] offset:32
	global_load_dwordx4 v[142:145], v3, s[82:83] offset:48
	s_add_u32 s82, s42, s4
	s_addc_u32 s83, s43, s5
	global_load_dwordx4 v[146:149], v3, s[82:83]
	global_load_dwordx4 v[150:153], v3, s[82:83] offset:16
	global_load_dwordx4 v[154:157], v3, s[82:83] offset:32
	global_load_dwordx4 v[158:161], v3, s[82:83] offset:48
	s_add_u32 s82, s20, s4
	s_addc_u32 s83, s33, s5
	global_load_dwordx4 v[162:165], v3, s[82:83]
	global_load_dwordx4 v[166:169], v3, s[82:83] offset:16
	global_load_dwordx4 v[170:173], v3, s[82:83] offset:32
	global_load_dwordx4 v[174:177], v3, s[82:83] offset:48
	global_load_dwordx2 v[178:179], v[42:43], off offset:-252
	global_load_dwordx2 v[182:183], v[42:43], off offset:-244
	global_load_dwordx2 v[184:185], v[42:43], off offset:4
	global_load_dwordx2 v[186:187], v[42:43], off offset:12
	s_add_u32 s82, s79, s4
	s_addc_u32 s83, s80, s5
	s_add_u32 s82, s82, 0x4000
	s_addc_u32 s83, s83, 0
	global_load_dwordx4 v[188:191], v3, s[82:83]
	global_load_dwordx4 v[192:195], v3, s[82:83] offset:16
	global_load_dwordx4 v[196:199], v3, s[82:83] offset:32
	global_load_dwordx4 v[200:203], v3, s[82:83] offset:48
	s_add_u32 s82, s44, s4
	s_addc_u32 s83, s45, s5
	s_add_u32 s82, s82, 0x4000
	s_addc_u32 s83, s83, 0
	global_load_dwordx4 v[204:207], v3, s[82:83]
	global_load_dwordx4 v[208:211], v3, s[82:83] offset:16
	global_load_dwordx4 v[212:215], v3, s[82:83] offset:32
	global_load_dwordx4 v[216:219], v3, s[82:83] offset:48
	s_add_u32 s82, s42, s4
	s_addc_u32 s83, s43, s5
	s_add_u32 s82, s82, 0x4000
	s_addc_u32 s83, s83, 0
	global_load_dwordx4 v[220:223], v3, s[82:83]
	global_load_dwordx4 v[224:227], v3, s[82:83] offset:16
	global_load_dwordx4 v[228:231], v3, s[82:83] offset:32
	global_load_dwordx4 v[232:235], v3, s[82:83] offset:48
	s_add_u32 s82, s20, s4
	s_addc_u32 s83, s33, s5
	s_add_u32 s82, s82, 0x4000
	s_addc_u32 s83, s83, 0
	global_load_dwordx4 v[236:239], v3, s[82:83]
	global_load_dwordx4 v[240:243], v3, s[82:83] offset:16
	global_load_dwordx4 v[244:247], v3, s[82:83] offset:32
	global_load_dwordx4 v[248:251], v3, s[82:83] offset:48
	v_lshl_add_u64 v[42:43], v[42:43], 0, 32
	s_add_u32 s4, s4, 0x8000
	s_addc_u32 s5, s5, 0
	s_cmp_lg_u32 s4, 0x40000
	s_waitcnt vmcnt(32)
	v_pk_fma_f32 v[74:75], v[80:81], v[120:121], v[74:75] op_sel_hi:[0,1,1]
	v_pk_fma_f32 v[72:73], v[76:77], v[120:121], v[72:73] op_sel_hi:[0,1,1]
	v_pk_fma_f32 v[70:71], v[80:81], v[122:123], v[70:71] op_sel_hi:[0,1,1]
	v_pk_fma_f32 v[68:69], v[76:77], v[122:123], v[68:69] op_sel_hi:[0,1,1]
	v_pk_fma_f32 v[66:67], v[80:81], v[116:117], v[66:67] op_sel_hi:[0,1,1]
	v_pk_fma_f32 v[64:65], v[76:77], v[116:117], v[64:65] op_sel_hi:[0,1,1]
	v_pk_fma_f32 v[62:63], v[80:81], v[118:119], v[62:63] op_sel_hi:[0,1,1]
	v_pk_fma_f32 v[60:61], v[76:77], v[118:119], v[60:61] op_sel_hi:[0,1,1]
	v_pk_fma_f32 v[58:59], v[80:81], v[112:113], v[58:59] op_sel_hi:[0,1,1]
	v_pk_fma_f32 v[56:57], v[76:77], v[112:113], v[56:57] op_sel_hi:[0,1,1]
	v_pk_fma_f32 v[54:55], v[80:81], v[114:115], v[54:55] op_sel_hi:[0,1,1]
	v_pk_fma_f32 v[52:53], v[76:77], v[114:115], v[52:53] op_sel_hi:[0,1,1]
	v_pk_fma_f32 v[50:51], v[80:81], v[108:109], v[50:51] op_sel_hi:[0,1,1]
	v_pk_fma_f32 v[48:49], v[76:77], v[108:109], v[48:49] op_sel_hi:[0,1,1]
	v_pk_fma_f32 v[46:47], v[80:81], v[110:111], v[46:47] op_sel_hi:[0,1,1]
	v_pk_fma_f32 v[44:45], v[76:77], v[110:111], v[44:45] op_sel_hi:[0,1,1]
	s_waitcnt vmcnt(28)
	v_pk_fma_f32 v[74:75], v[80:81], v[130:131], v[74:75] op_sel:[1,0,0]
	v_pk_fma_f32 v[72:73], v[76:77], v[130:131], v[72:73] op_sel:[1,0,0]
	v_pk_fma_f32 v[70:71], v[80:81], v[132:133], v[70:71] op_sel:[1,0,0]
	v_pk_fma_f32 v[68:69], v[76:77], v[132:133], v[68:69] op_sel:[1,0,0]
	v_pk_fma_f32 v[66:67], v[80:81], v[134:135], v[66:67] op_sel:[1,0,0]
	v_pk_fma_f32 v[64:65], v[76:77], v[134:135], v[64:65] op_sel:[1,0,0]
	v_pk_fma_f32 v[62:63], v[80:81], v[136:137], v[62:63] op_sel:[1,0,0]
	v_pk_fma_f32 v[60:61], v[76:77], v[136:137], v[60:61] op_sel:[1,0,0]
	v_pk_fma_f32 v[58:59], v[80:81], v[138:139], v[58:59] op_sel:[1,0,0]
	v_pk_fma_f32 v[56:57], v[76:77], v[138:139], v[56:57] op_sel:[1,0,0]
	v_pk_fma_f32 v[54:55], v[80:81], v[140:141], v[54:55] op_sel:[1,0,0]
	v_pk_fma_f32 v[52:53], v[76:77], v[140:141], v[52:53] op_sel:[1,0,0]
	v_pk_fma_f32 v[50:51], v[80:81], v[142:143], v[50:51] op_sel:[1,0,0]
	v_pk_fma_f32 v[48:49], v[76:77], v[142:143], v[48:49] op_sel:[1,0,0]
	v_pk_fma_f32 v[46:47], v[80:81], v[144:145], v[46:47] op_sel:[1,0,0]
	v_pk_fma_f32 v[44:45], v[76:77], v[144:145], v[44:45] op_sel:[1,0,0]
	s_waitcnt vmcnt(24)
	v_pk_fma_f32 v[74:75], v[82:83], v[146:147], v[74:75] op_sel_hi:[0,1,1]
	v_pk_fma_f32 v[72:73], v[78:79], v[146:147], v[72:73] op_sel_hi:[0,1,1]
	v_pk_fma_f32 v[70:71], v[82:83], v[148:149], v[70:71] op_sel_hi:[0,1,1]
	v_pk_fma_f32 v[68:69], v[78:79], v[148:149], v[68:69] op_sel_hi:[0,1,1]
	v_pk_fma_f32 v[66:67], v[82:83], v[150:151], v[66:67] op_sel_hi:[0,1,1]
	v_pk_fma_f32 v[64:65], v[78:79], v[150:151], v[64:65] op_sel_hi:[0,1,1]
	v_pk_fma_f32 v[62:63], v[82:83], v[152:153], v[62:63] op_sel_hi:[0,1,1]
	v_pk_fma_f32 v[60:61], v[78:79], v[152:153], v[60:61] op_sel_hi:[0,1,1]
	v_pk_fma_f32 v[58:59], v[82:83], v[154:155], v[58:59] op_sel_hi:[0,1,1]
	v_pk_fma_f32 v[56:57], v[78:79], v[154:155], v[56:57] op_sel_hi:[0,1,1]
	v_pk_fma_f32 v[54:55], v[82:83], v[156:157], v[54:55] op_sel_hi:[0,1,1]
	v_pk_fma_f32 v[52:53], v[78:79], v[156:157], v[52:53] op_sel_hi:[0,1,1]
	v_pk_fma_f32 v[50:51], v[82:83], v[158:159], v[50:51] op_sel_hi:[0,1,1]
	v_pk_fma_f32 v[48:49], v[78:79], v[158:159], v[48:49] op_sel_hi:[0,1,1]
	v_pk_fma_f32 v[46:47], v[82:83], v[160:161], v[46:47] op_sel_hi:[0,1,1]
	v_pk_fma_f32 v[44:45], v[78:79], v[160:161], v[44:45] op_sel_hi:[0,1,1]
	s_waitcnt vmcnt(20)
	v_pk_fma_f32 v[74:75], v[82:83], v[162:163], v[74:75] op_sel:[1,0,0]
	v_pk_fma_f32 v[72:73], v[78:79], v[162:163], v[72:73] op_sel:[1,0,0]
	v_pk_fma_f32 v[70:71], v[82:83], v[164:165], v[70:71] op_sel:[1,0,0]
	v_pk_fma_f32 v[68:69], v[78:79], v[164:165], v[68:69] op_sel:[1,0,0]
	v_pk_fma_f32 v[66:67], v[82:83], v[166:167], v[66:67] op_sel:[1,0,0]
	v_pk_fma_f32 v[64:65], v[78:79], v[166:167], v[64:65] op_sel:[1,0,0]
	v_pk_fma_f32 v[62:63], v[82:83], v[168:169], v[62:63] op_sel:[1,0,0]
	v_pk_fma_f32 v[60:61], v[78:79], v[168:169], v[60:61] op_sel:[1,0,0]
	v_pk_fma_f32 v[58:59], v[82:83], v[170:171], v[58:59] op_sel:[1,0,0]
	v_pk_fma_f32 v[56:57], v[78:79], v[170:171], v[56:57] op_sel:[1,0,0]
	v_pk_fma_f32 v[54:55], v[82:83], v[172:173], v[54:55] op_sel:[1,0,0]
	v_pk_fma_f32 v[52:53], v[78:79], v[172:173], v[52:53] op_sel:[1,0,0]
	v_pk_fma_f32 v[50:51], v[82:83], v[174:175], v[50:51] op_sel:[1,0,0]
	v_pk_fma_f32 v[48:49], v[78:79], v[174:175], v[48:49] op_sel:[1,0,0]
	v_pk_fma_f32 v[46:47], v[82:83], v[176:177], v[46:47] op_sel:[1,0,0]
	v_pk_fma_f32 v[44:45], v[78:79], v[176:177], v[44:45] op_sel:[1,0,0]
	s_waitcnt vmcnt(12)
	v_pk_fma_f32 v[74:75], v[184:185], v[188:189], v[74:75] op_sel_hi:[0,1,1]
	v_pk_fma_f32 v[72:73], v[178:179], v[188:189], v[72:73] op_sel_hi:[0,1,1]
	v_pk_fma_f32 v[70:71], v[184:185], v[190:191], v[70:71] op_sel_hi:[0,1,1]
	v_pk_fma_f32 v[68:69], v[178:179], v[190:191], v[68:69] op_sel_hi:[0,1,1]
	v_pk_fma_f32 v[66:67], v[184:185], v[192:193], v[66:67] op_sel_hi:[0,1,1]
	v_pk_fma_f32 v[64:65], v[178:179], v[192:193], v[64:65] op_sel_hi:[0,1,1]
	v_pk_fma_f32 v[62:63], v[184:185], v[194:195], v[62:63] op_sel_hi:[0,1,1]
	v_pk_fma_f32 v[60:61], v[178:179], v[194:195], v[60:61] op_sel_hi:[0,1,1]
	v_pk_fma_f32 v[58:59], v[184:185], v[196:197], v[58:59] op_sel_hi:[0,1,1]
	v_pk_fma_f32 v[56:57], v[178:179], v[196:197], v[56:57] op_sel_hi:[0,1,1]
	v_pk_fma_f32 v[54:55], v[184:185], v[198:199], v[54:55] op_sel_hi:[0,1,1]
	v_pk_fma_f32 v[52:53], v[178:179], v[198:199], v[52:53] op_sel_hi:[0,1,1]
	v_pk_fma_f32 v[50:51], v[184:185], v[200:201], v[50:51] op_sel_hi:[0,1,1]
	v_pk_fma_f32 v[48:49], v[178:179], v[200:201], v[48:49] op_sel_hi:[0,1,1]
	v_pk_fma_f32 v[46:47], v[184:185], v[202:203], v[46:47] op_sel_hi:[0,1,1]
	v_pk_fma_f32 v[44:45], v[178:179], v[202:203], v[44:45] op_sel_hi:[0,1,1]
	s_waitcnt vmcnt(8)
	v_pk_fma_f32 v[74:75], v[184:185], v[204:205], v[74:75] op_sel:[1,0,0]
	v_pk_fma_f32 v[72:73], v[178:179], v[204:205], v[72:73] op_sel:[1,0,0]
	v_pk_fma_f32 v[70:71], v[184:185], v[206:207], v[70:71] op_sel:[1,0,0]
	v_pk_fma_f32 v[68:69], v[178:179], v[206:207], v[68:69] op_sel:[1,0,0]
	v_pk_fma_f32 v[66:67], v[184:185], v[208:209], v[66:67] op_sel:[1,0,0]
	v_pk_fma_f32 v[64:65], v[178:179], v[208:209], v[64:65] op_sel:[1,0,0]
	v_pk_fma_f32 v[62:63], v[184:185], v[210:211], v[62:63] op_sel:[1,0,0]
	v_pk_fma_f32 v[60:61], v[178:179], v[210:211], v[60:61] op_sel:[1,0,0]
	v_pk_fma_f32 v[58:59], v[184:185], v[212:213], v[58:59] op_sel:[1,0,0]
	v_pk_fma_f32 v[56:57], v[178:179], v[212:213], v[56:57] op_sel:[1,0,0]
	v_pk_fma_f32 v[54:55], v[184:185], v[214:215], v[54:55] op_sel:[1,0,0]
	v_pk_fma_f32 v[52:53], v[178:179], v[214:215], v[52:53] op_sel:[1,0,0]
	v_pk_fma_f32 v[50:51], v[184:185], v[216:217], v[50:51] op_sel:[1,0,0]
	v_pk_fma_f32 v[48:49], v[178:179], v[216:217], v[48:49] op_sel:[1,0,0]
	v_pk_fma_f32 v[46:47], v[184:185], v[218:219], v[46:47] op_sel:[1,0,0]
	v_pk_fma_f32 v[44:45], v[178:179], v[218:219], v[44:45] op_sel:[1,0,0]
	s_waitcnt vmcnt(4)
	v_pk_fma_f32 v[74:75], v[186:187], v[220:221], v[74:75] op_sel_hi:[0,1,1]
	v_pk_fma_f32 v[72:73], v[182:183], v[220:221], v[72:73] op_sel_hi:[0,1,1]
	v_pk_fma_f32 v[70:71], v[186:187], v[222:223], v[70:71] op_sel_hi:[0,1,1]
	v_pk_fma_f32 v[68:69], v[182:183], v[222:223], v[68:69] op_sel_hi:[0,1,1]
	v_pk_fma_f32 v[66:67], v[186:187], v[224:225], v[66:67] op_sel_hi:[0,1,1]
	v_pk_fma_f32 v[64:65], v[182:183], v[224:225], v[64:65] op_sel_hi:[0,1,1]
	v_pk_fma_f32 v[62:63], v[186:187], v[226:227], v[62:63] op_sel_hi:[0,1,1]
	v_pk_fma_f32 v[60:61], v[182:183], v[226:227], v[60:61] op_sel_hi:[0,1,1]
	v_pk_fma_f32 v[58:59], v[186:187], v[228:229], v[58:59] op_sel_hi:[0,1,1]
	v_pk_fma_f32 v[56:57], v[182:183], v[228:229], v[56:57] op_sel_hi:[0,1,1]
	v_pk_fma_f32 v[54:55], v[186:187], v[230:231], v[54:55] op_sel_hi:[0,1,1]
	v_pk_fma_f32 v[52:53], v[182:183], v[230:231], v[52:53] op_sel_hi:[0,1,1]
	v_pk_fma_f32 v[50:51], v[186:187], v[232:233], v[50:51] op_sel_hi:[0,1,1]
	v_pk_fma_f32 v[48:49], v[182:183], v[232:233], v[48:49] op_sel_hi:[0,1,1]
	v_pk_fma_f32 v[46:47], v[186:187], v[234:235], v[46:47] op_sel_hi:[0,1,1]
	v_pk_fma_f32 v[44:45], v[182:183], v[234:235], v[44:45] op_sel_hi:[0,1,1]
	s_waitcnt vmcnt(0)
	v_pk_fma_f32 v[74:75], v[186:187], v[236:237], v[74:75] op_sel:[1,0,0]
	v_pk_fma_f32 v[72:73], v[182:183], v[236:237], v[72:73] op_sel:[1,0,0]
	v_pk_fma_f32 v[70:71], v[186:187], v[238:239], v[70:71] op_sel:[1,0,0]
	v_pk_fma_f32 v[68:69], v[182:183], v[238:239], v[68:69] op_sel:[1,0,0]
	v_pk_fma_f32 v[66:67], v[186:187], v[240:241], v[66:67] op_sel:[1,0,0]
	v_pk_fma_f32 v[64:65], v[182:183], v[240:241], v[64:65] op_sel:[1,0,0]
	v_pk_fma_f32 v[62:63], v[186:187], v[242:243], v[62:63] op_sel:[1,0,0]
	v_pk_fma_f32 v[60:61], v[182:183], v[242:243], v[60:61] op_sel:[1,0,0]
	v_pk_fma_f32 v[58:59], v[186:187], v[244:245], v[58:59] op_sel:[1,0,0]
	v_pk_fma_f32 v[56:57], v[182:183], v[244:245], v[56:57] op_sel:[1,0,0]
	v_pk_fma_f32 v[54:55], v[186:187], v[246:247], v[54:55] op_sel:[1,0,0]
	v_pk_fma_f32 v[52:53], v[182:183], v[246:247], v[52:53] op_sel:[1,0,0]
	v_pk_fma_f32 v[50:51], v[186:187], v[248:249], v[50:51] op_sel:[1,0,0]
	v_pk_fma_f32 v[48:49], v[182:183], v[248:249], v[48:49] op_sel:[1,0,0]
	v_pk_fma_f32 v[46:47], v[186:187], v[250:251], v[46:47] op_sel:[1,0,0]
	v_pk_fma_f32 v[44:45], v[182:183], v[250:251], v[44:45] op_sel:[1,0,0]
	s_cbranch_scc1 .LBB0_49
	s_add_i32 s4, s78, 0xfffff990
	s_lshl_b32 s5, s4, 4
	s_lshl_b32 s4, s4, 2
	v_bfe_u32 v2, v72, 16, 1
	s_and_b32 s5, s5, 0x3f0
	s_and_b32 s20, s4, 0x700
	v_add3_u32 v2, v72, v2, s70
	v_bfe_u32 v33, v74, 16, 1
	v_lshl_add_u64 v[42:43], v[28:29], 0, s[20:21]
	v_lshrrev_b32_e32 v2, 16, v2
	v_add3_u32 v33, v74, v33, s70
	s_mul_i32 s20, s5, 0xc00
	v_and_or_b32 v2, v33, s71, v2
	v_lshl_add_u64 v[42:43], v[42:43], 0, s[20:21]
	global_store_dword v[42:43], v2, off
	v_bfe_u32 v2, v73, 16, 1
	v_add3_u32 v2, v73, v2, s70
	v_bfe_u32 v33, v75, 16, 1
	v_lshrrev_b32_e32 v2, 16, v2
	v_add3_u32 v33, v75, v33, s70
	v_and_or_b32 v2, v33, s71, v2
	global_store_dword v[42:43], v2, off offset:3072
	v_bfe_u32 v2, v68, 16, 1
	v_add3_u32 v2, v68, v2, s70
	v_bfe_u32 v33, v70, 16, 1
	v_lshrrev_b32_e32 v2, 16, v2
	v_add3_u32 v33, v70, v33, s70
	v_add_co_u32_e32 v72, vcc, s72, v42
	v_and_or_b32 v2, v33, s71, v2
	s_nop 0
	v_addc_co_u32_e32 v73, vcc, 0, v43, vcc
	global_store_dword v[72:73], v2, off offset:2048
	v_bfe_u32 v2, v69, 16, 1
	v_add3_u32 v2, v69, v2, s70
	v_bfe_u32 v33, v71, 16, 1
	v_lshrrev_b32_e32 v2, 16, v2
	v_add3_u32 v33, v71, v33, s70
	v_add_co_u32_e32 v68, vcc, s55, v42
	v_and_or_b32 v2, v33, s71, v2
	s_nop 0
	v_addc_co_u32_e32 v69, vcc, 0, v43, vcc
	global_store_dword v[68:69], v2, off offset:1024
	v_bfe_u32 v2, v64, 16, 1
	v_add3_u32 v2, v64, v2, s70
	v_bfe_u32 v33, v66, 16, 1
	v_lshrrev_b32_e32 v2, 16, v2
	v_add3_u32 v33, v66, v33, s70
	v_add_co_u32_e32 v68, vcc, s73, v42
	v_and_or_b32 v2, v33, s71, v2
	s_nop 0
	v_addc_co_u32_e32 v69, vcc, 0, v43, vcc
	global_store_dword v[68:69], v2, off
	v_bfe_u32 v2, v65, 16, 1
	v_add3_u32 v2, v65, v2, s70
	v_bfe_u32 v33, v67, 16, 1
	v_lshrrev_b32_e32 v2, 16, v2
	v_add3_u32 v33, v67, v33, s70
	v_and_or_b32 v2, v33, s71, v2
	global_store_dword v[68:69], v2, off offset:3072
	v_bfe_u32 v2, v60, 16, 1
	v_add3_u32 v2, v60, v2, s70
	v_bfe_u32 v33, v62, 16, 1
	v_lshrrev_b32_e32 v2, 16, v2
	v_add3_u32 v33, v62, v33, s70
	v_add_co_u32_e32 v64, vcc, s56, v42
	v_and_or_b32 v2, v33, s71, v2
	s_nop 0
	v_addc_co_u32_e32 v65, vcc, 0, v43, vcc
	global_store_dword v[64:65], v2, off offset:2048
	v_bfe_u32 v2, v61, 16, 1
	v_add3_u32 v2, v61, v2, s70
	v_bfe_u32 v33, v63, 16, 1
	v_lshrrev_b32_e32 v2, 16, v2
	v_add3_u32 v33, v63, v33, s70
	v_add_co_u32_e32 v60, vcc, s74, v42
	v_and_or_b32 v2, v33, s71, v2
	s_nop 0
	v_addc_co_u32_e32 v61, vcc, 0, v43, vcc
	global_store_dword v[60:61], v2, off offset:1024
	v_bfe_u32 v2, v56, 16, 1
	v_add3_u32 v2, v56, v2, s70
	v_bfe_u32 v33, v58, 16, 1
	v_lshrrev_b32_e32 v2, 16, v2
	v_add3_u32 v33, v58, v33, s70
	v_add_co_u32_e32 v60, vcc, s57, v42
	v_and_or_b32 v2, v33, s71, v2
	s_nop 0
	v_addc_co_u32_e32 v61, vcc, 0, v43, vcc
	global_store_dword v[60:61], v2, off
	v_bfe_u32 v2, v57, 16, 1
	v_add3_u32 v2, v57, v2, s70
	v_bfe_u32 v33, v59, 16, 1
	v_lshrrev_b32_e32 v2, 16, v2
	v_add3_u32 v33, v59, v33, s70
	v_and_or_b32 v2, v33, s71, v2
	global_store_dword v[60:61], v2, off offset:3072
	v_bfe_u32 v2, v52, 16, 1
	v_add3_u32 v2, v52, v2, s70
	v_bfe_u32 v33, v54, 16, 1
	v_lshrrev_b32_e32 v2, 16, v2
	v_add3_u32 v33, v54, v33, s70
	v_add_co_u32_e32 v56, vcc, s75, v42
	v_and_or_b32 v2, v33, s71, v2
	s_nop 0
	v_addc_co_u32_e32 v57, vcc, 0, v43, vcc
	global_store_dword v[56:57], v2, off offset:2048
	v_bfe_u32 v2, v53, 16, 1
	v_add3_u32 v2, v53, v2, s70
	v_bfe_u32 v33, v55, 16, 1
	v_lshrrev_b32_e32 v2, 16, v2
	v_add3_u32 v33, v55, v33, s70
	v_add_co_u32_e32 v52, vcc, s58, v42
	v_and_or_b32 v2, v33, s71, v2
	s_nop 0
	v_addc_co_u32_e32 v53, vcc, 0, v43, vcc
	global_store_dword v[52:53], v2, off offset:1024
	v_bfe_u32 v2, v48, 16, 1
	v_add3_u32 v2, v48, v2, s70
	v_bfe_u32 v33, v50, 16, 1
	v_lshrrev_b32_e32 v2, 16, v2
	v_add3_u32 v33, v50, v33, s70
	v_add_co_u32_e32 v52, vcc, s76, v42
	v_and_or_b32 v2, v33, s71, v2
	s_nop 0
	v_addc_co_u32_e32 v53, vcc, 0, v43, vcc
	global_store_dword v[52:53], v2, off
	v_bfe_u32 v2, v49, 16, 1
	v_add3_u32 v2, v49, v2, s70
	v_bfe_u32 v33, v51, 16, 1
	v_lshrrev_b32_e32 v2, 16, v2
	v_add3_u32 v33, v51, v33, s70
	v_and_or_b32 v2, v33, s71, v2
	global_store_dword v[52:53], v2, off offset:3072
	v_bfe_u32 v2, v44, 16, 1
	v_add3_u32 v2, v44, v2, s70
	v_bfe_u32 v33, v46, 16, 1
	v_lshrrev_b32_e32 v2, 16, v2
	v_add3_u32 v33, v46, v33, s70
	v_add_co_u32_e32 v48, vcc, s59, v42
	v_and_or_b32 v2, v33, s71, v2
	s_nop 0
	v_addc_co_u32_e32 v49, vcc, 0, v43, vcc
	global_store_dword v[48:49], v2, off offset:2048
	v_bfe_u32 v2, v45, 16, 1
	v_add3_u32 v2, v45, v2, s70
	v_bfe_u32 v33, v47, 16, 1
	v_lshrrev_b32_e32 v2, 16, v2
	v_add3_u32 v33, v47, v33, s70
	v_add_co_u32_e32 v42, vcc, 0xb000, v42
	v_and_or_b32 v2, v33, s71, v2
	s_nop 0
	v_addc_co_u32_e32 v43, vcc, 0, v43, vcc
	global_store_dword v[42:43], v2, off offset:1024
